# scan phase: static s_setprio 3 for the four scanner waves (dependency-chain bound) over the loader waves sharing their SIMDs
# baseline (speedup 1.0000x reference)
.LBB0_604:
	s_ashr_i32 s1, s57, 2
	s_and_b32 s0, s57, 7
	s_and_b32 s1, s1, -8
	s_or_b32 s0, s1, s0
	s_ashr_i32 s1, s0, 1
	s_lshr_b32 s6, s1, 30
	s_add_i32 s6, s1, s6
	s_and_b32 s6, s6, -4
	s_waitcnt lgkmcnt(0)
	s_sub_i32 s51, s1, s6
	s_ashr_i32 s1, s57, 31
	s_lshr_b32 s1, s1, 29
	s_add_i32 s0, s0, s1
	s_bfe_u32 s7, s57, 0x20003
	s_and_b32 s50, s57, 1
	s_ashr_i32 s6, s0, 3
	s_mov_b64 s[0:1], -1
	s_and_b64 vcc, exec, s[64:65]
	s_barrier
	s_cbranch_vccz .LBB0_617
	s_setprio 3
	s_load_dwordx2 s[0:1], s[58:59], 0x1e8
	s_mul_i32 s8, s50, 0x1100000
	v_mov_b32_e32 v14, 0
	v_bfrev_b32_e32 v89, v85
	v_and_b32_e32 v112, 2, v85
	v_and_b32_e32 v113, 1, v85
	v_lshrrev_b32_e32 v89, 28, v89
	v_cmp_ne_u32_e64 s[14:15], 0, v112
	v_cmp_ne_u32_e64 s[16:17], 0, v113
	v_or_b32_e32 v94, 16, v89
	s_cmp_lg_u32 s50, 0
	s_cselect_b32 s20, -32, 32
	s_cselect_b32 s21, 0xfff, 0
	s_lshl_b32 s22, s6, 12
	s_add_i32 s21, s21, s22
	v_mov_b32_e32 v15, v14
	v_mov_b32_e32 v16, v14
	s_waitcnt lgkmcnt(0)
	s_add_u32 s8, s0, s8
	s_addc_u32 s9, s1, 0
	s_lshl_b32 s0, s51, 6
	s_ashr_i32 s1, s0, 31
	s_lshl_b64 s[0:1], s[0:1], 1
	s_add_u32 s0, s8, s0
	s_addc_u32 s1, s9, s1
	s_lshl_b32 s8, s7, 5
	s_add_u32 s0, s0, s8
	s_addc_u32 s1, s1, 0
	s_cmp_lg_u32 s50, 0
	v_lshl_add_u64 v[10:11], v[82:83], 1, s[0:1]
	s_cselect_b64 s[0:1], -1, 0
	s_lshl_b32 s70, s6, 12
	s_lshl_b32 s33, s6, 8
	s_mov_b32 s8, 0
	s_add_i32 s9, s70, 0x10ff
	s_add_i32 s52, s33, 0x80ff
	s_addk_i32 s70, 0xff00
	s_add_i32 s71, s33, 0x8000
	v_mov_b32_e32 v17, v14
	s_barrier
	v_mov_b32_e32 v18, v87
	v_add_u32_e32 v2, 0xa000, v96
	ds_read_b128 v[20:23], v18
	ds_read_b128 v[28:31], v18 offset:24576
	ds_read2_b32 v[120:121], v2 offset1:16
	ds_read_b128 v[24:27], v18 offset:8192
	ds_read_b128 v[32:35], v18 offset:32768
	ds_read_b128 v[36:39], v18 offset:256
	ds_read_b128 v[44:47], v18 offset:24832
	ds_read_b128 v[40:43], v18 offset:8448
	ds_read_b128 v[48:51], v18 offset:33024
	s_branch .LBB0_608

.LBB0_618:
	s_waitcnt lgkmcnt(0)
	s_waitcnt lgkmcnt(9)
	v_pk_mul_f32 v[128:129], v[14:15], v[112:113]
	s_nop 0
	v_pk_fma_f32 v[128:129], v[16:17], v[114:115], v[128:129]
	s_nop 0
	v_add_f32_e32 v131, v128, v129
	v_add_f32_dpp v133, v130, v130 row_mirror row_mask:0xf bank_mask:0x3 bound_ctrl:1
	s_nop 0
	v_add_f32_dpp v133, v131, v131 row_mirror row_mask:0xf bank_mask:0xc bound_ctrl:1
	v_add_f32_dpp v135, v132, v132 row_half_mirror row_mask:0xf bank_mask:0x5 bound_ctrl:1
	s_nop 0
	v_add_f32_dpp v135, v133, v133 row_half_mirror row_mask:0xf bank_mask:0xa bound_ctrl:1
	v_add_f32_dpp v138, v134, v134 quad_perm:[2,3,0,1] row_mask:0xf bank_mask:0xf bound_ctrl:1
	s_nop 0
	v_add_f32_dpp v98, v135, v135 quad_perm:[2,3,0,1] row_mask:0xf bank_mask:0xf bound_ctrl:1
	v_cndmask_b32_e64 v137, v138, v98, s[14:15]
	v_add_f32_dpp v138, v136, v136 quad_perm:[1,0,3,2] row_mask:0xf bank_mask:0xf bound_ctrl:1
	s_nop 0
	v_add_f32_dpp v98, v137, v137 quad_perm:[1,0,3,2] row_mask:0xf bank_mask:0xf bound_ctrl:1
	v_cndmask_b32_e64 v99, v138, v98, s[16:17]
	v_bfe_u32 v7, v99, 16, 1
	v_add3_u32 v7, v99, v7, s3
	global_store_short_d16_hi v[8:9], v7, off
	s_setprio 0
	s_branch .LBB0_603
